# v49 + near-tie path de-serialised: all candidate codebook-row loads issued up front at slow-path entry
# speedup vs baseline: 1.0179x; 1.0179x over previous
.Lg_alldone:
	s_cmp_lg_u32 s17, 0
	s_cbranch_scc1 .Lg_nocopy
	v_cmp_gt_u32_e32 vcc, 16, v1
	s_and_saveexec_b64 s[30:31], vcc
	v_mul_u32_u24_e32 v220, 0x810, v1
	ds_read_b32 v221, v220 offset:34816
	v_mov_b32_e32 v144, 0x11100
	v_lshl_add_u32 v220, v1, 2, v144
	s_waitcnt lgkmcnt(0)
	ds_write_b32 v220, v221
	s_mov_b64 exec, s[30:31]

.LBB0_118:
	s_waitcnt vmcnt(0)
	v_lshrrev_b32_e32 v67, 4, v0
	v_mov_b32_e32 v66, 0x11100
	v_lshl_or_b32 v66, v67, 2, v66
	s_waitcnt lgkmcnt(0)
	s_barrier
	ds_read_b32 v66, v66
	v_mul_u32_u24_e32 v68, 0x102, v67
	v_lshlrev_b32_e32 v72, 3, v68
	s_waitcnt lgkmcnt(0)
	v_max_i32_e32 v66, 1, v66
	v_cvt_f32_u32_e32 v66, v66
	v_div_scale_f32 v69, s[0:1], v66, v66, 1.0
	v_rcp_f32_e32 v70, v69
	v_div_scale_f32 v68, vcc, 1.0, v66, 1.0
	v_fma_f32 v71, -v69, v70, 1.0
	v_fmac_f32_e32 v70, v71, v70
	v_mul_f32_e32 v71, v68, v70
	v_fma_f32 v73, -v69, v71, v68
	v_fmac_f32_e32 v71, v73, v70
	v_fma_f32 v68, -v69, v71, v68
	v_div_fmas_f32 v73, v68, v70, v71
	v_lshl_add_u32 v68, v138, 3, v72
	v_add_u32_e32 v76, 0x8000, v68
	ds_read2_b64 v[68:71], v76 offset1:16
	v_div_fixup_f32 v77, v73, v66, 1.0
	v_mul_i32_i24_e32 v73, 0xfffffbf8, v67
	v_lshlrev_b32_e32 v66, 2, v138
	v_add3_u32 v78, v72, v73, v66
	ds_read2_b64 v[72:75], v76 offset0:32 offset1:48
	s_waitcnt lgkmcnt(1)
	v_cvt_f32_f64_e32 v68, v[68:69]
	v_cvt_f32_f64_e32 v69, v[70:71]
	v_mul_f32_e32 v68, v77, v68
	v_mul_f32_e32 v69, v77, v69
	v_fma_f32 v79, v68, v68, 0
	ds_write2_b32 v78, v68, v69 offset1:16
	s_waitcnt lgkmcnt(1)
	v_cvt_f32_f64_e32 v68, v[72:73]
	v_fmac_f32_e32 v79, v69, v69
	v_mul_f32_e32 v72, v77, v68
	ds_read2_b64 v[68:71], v76 offset0:64 offset1:80
	v_cvt_f32_f64_e32 v73, v[74:75]
	v_fmac_f32_e32 v79, v72, v72
	v_mul_f32_e32 v73, v77, v73
	v_fmac_f32_e32 v79, v73, v73
	ds_write2_b32 v78, v72, v73 offset0:32 offset1:48
	ds_read2_b64 v[72:75], v76 offset0:96 offset1:112
	s_waitcnt lgkmcnt(2)
	v_cvt_f32_f64_e32 v68, v[68:69]
	v_cvt_f32_f64_e32 v69, v[70:71]
	v_mul_f32_e32 v68, v77, v68
	v_mul_f32_e32 v69, v77, v69
	v_fmac_f32_e32 v79, v68, v68
	ds_write2_b32 v78, v68, v69 offset0:64 offset1:80
	s_waitcnt lgkmcnt(1)
	v_cvt_f32_f64_e32 v68, v[72:73]
	v_fmac_f32_e32 v79, v69, v69
	v_mul_f32_e32 v72, v77, v68
	ds_read2_b64 v[68:71], v76 offset0:128 offset1:144
	v_cvt_f32_f64_e32 v73, v[74:75]
	v_fmac_f32_e32 v79, v72, v72
	v_mul_f32_e32 v73, v77, v73
	v_fmac_f32_e32 v79, v73, v73
	ds_write2_b32 v78, v72, v73 offset0:96 offset1:112
	ds_read2_b64 v[72:75], v76 offset0:160 offset1:176
	s_waitcnt lgkmcnt(2)
	v_cvt_f32_f64_e32 v68, v[68:69]
	v_cvt_f32_f64_e32 v69, v[70:71]
	v_mul_f32_e32 v68, v77, v68
	v_mul_f32_e32 v69, v77, v69
	v_fmac_f32_e32 v79, v68, v68
	ds_write2_b32 v78, v68, v69 offset0:128 offset1:144
	s_waitcnt lgkmcnt(1)
	v_cvt_f32_f64_e32 v68, v[72:73]
	v_fmac_f32_e32 v79, v69, v69
	v_mul_f32_e32 v72, v77, v68
	ds_read2_b64 v[68:71], v76 offset0:192 offset1:208
	v_cvt_f32_f64_e32 v73, v[74:75]
	v_fmac_f32_e32 v79, v72, v72
	v_mul_f32_e32 v73, v77, v73
	v_fmac_f32_e32 v79, v73, v73
	ds_write2_b32 v78, v72, v73 offset0:160 offset1:176
	ds_read2_b64 v[72:75], v76 offset0:224 offset1:240
	s_waitcnt lgkmcnt(2)
	v_cvt_f32_f64_e32 v68, v[68:69]
	v_cvt_f32_f64_e32 v69, v[70:71]
	v_mul_f32_e32 v68, v77, v68
	v_mul_f32_e32 v69, v77, v69
	v_fmac_f32_e32 v79, v68, v68
	ds_write2_b32 v78, v68, v69 offset0:192 offset1:208
	s_waitcnt lgkmcnt(1)
	v_cvt_f32_f64_e32 v68, v[72:73]
	v_fmac_f32_e32 v79, v69, v69
	v_mul_f32_e32 v68, v77, v68
	v_cvt_f32_f64_e32 v69, v[74:75]
	v_fmac_f32_e32 v79, v68, v68
	v_mul_f32_e32 v69, v77, v69
	v_fmac_f32_e32 v79, v69, v69
	ds_write2_b32 v78, v68, v69 offset0:224 offset1:240
	v_cmp_eq_u32_e32 vcc, 0, v138
	v_add_f32_dpp v68, v79, v79 quad_perm:[1,0,3,2] row_mask:0xf bank_mask:0xf bound_ctrl:1
	s_nop 1
	v_add_f32_dpp v68, v68, v68 quad_perm:[2,3,0,1] row_mask:0xf bank_mask:0xf bound_ctrl:1
	s_nop 1
	v_add_f32_dpp v68, v68, v68 row_half_mirror row_mask:0xf bank_mask:0xf bound_ctrl:1
	s_nop 1
	v_mov_b32_dpp v69, v68 row_mirror row_mask:0xf bank_mask:0xf bound_ctrl:1
	s_and_saveexec_b64 s[0:1], vcc
	v_mov_b32_e32 v70, 0x11200
	v_lshl_or_b32 v67, v67, 2, v70
	v_add_f32_e32 v68, v68, v69
	ds_write_b32 v67, v68
	s_or_b64 exec, exec, s[0:1]
	v_lshlrev_b32_e32 v67, 2, v140
	s_movk_i32 s0, 0x408
	v_mad_u32_u24 v67, v138, s0, v67
	s_waitcnt lgkmcnt(0)
	s_barrier
	ds_read2_b32 v[68:69], v67 offset1:4
	ds_read2_b32 v[70:71], v67 offset0:64 offset1:68
	ds_read2_b32 v[72:73], v67 offset0:192 offset1:196
	s_lshl_b32 s29, s17, 2
	s_lshl_b32 s0, s24, 2
	s_waitcnt lgkmcnt(2)
	v_mfma_f32_16x16x4_f32 a[0:3], v68, v62, 0
	s_add_i32 s0, s0, 0x10100
	s_waitcnt lgkmcnt(1)
	v_mfma_f32_16x16x4_f32 a[4:7], v70, v63, 0
	ds_read2_b32 v[62:63], v67 offset0:128 offset1:132
	s_waitcnt lgkmcnt(0)
	v_mfma_f32_16x16x4_f32 a[0:3], v62, v64, a[0:3]
	v_mfma_f32_16x16x4_f32 a[4:7], v72, v65, a[4:7]
	v_mfma_f32_16x16x4_f32 a[0:3], v69, v58, a[0:3]
	v_mfma_f32_16x16x4_f32 a[4:7], v71, v59, a[4:7]
	ds_read2_b32 v[58:59], v67 offset0:8 offset1:12
	v_mfma_f32_16x16x4_f32 a[0:3], v63, v60, a[0:3]
	ds_read2_b32 v[62:63], v67 offset0:200 offset1:204
	v_mfma_f32_16x16x4_f32 a[4:7], v73, v61, a[4:7]
	ds_read2_b32 v[60:61], v67 offset0:72 offset1:76
	s_waitcnt lgkmcnt(2)
	v_mfma_f32_16x16x4_f32 a[0:3], v58, v54, a[0:3]
	s_waitcnt lgkmcnt(0)
	v_mfma_f32_16x16x4_f32 a[4:7], v60, v55, a[4:7]
	ds_read2_b32 v[54:55], v67 offset0:136 offset1:140
	s_waitcnt lgkmcnt(0)
	v_mfma_f32_16x16x4_f32 a[0:3], v54, v56, a[0:3]
	v_mfma_f32_16x16x4_f32 a[4:7], v62, v57, a[4:7]
	v_mfma_f32_16x16x4_f32 a[0:3], v59, v50, a[0:3]
	v_mfma_f32_16x16x4_f32 a[4:7], v61, v51, a[4:7]
	ds_read2_b32 v[50:51], v67 offset0:16 offset1:20
	v_mfma_f32_16x16x4_f32 a[0:3], v55, v52, a[0:3]
	ds_read2_b32 v[54:55], v67 offset0:208 offset1:212
	v_mfma_f32_16x16x4_f32 a[4:7], v63, v53, a[4:7]
	ds_read2_b32 v[52:53], v67 offset0:80 offset1:84
	s_waitcnt lgkmcnt(2)
	v_mfma_f32_16x16x4_f32 a[0:3], v50, v46, a[0:3]
	s_waitcnt lgkmcnt(0)
	v_mfma_f32_16x16x4_f32 a[4:7], v52, v47, a[4:7]
	ds_read2_b32 v[46:47], v67 offset0:144 offset1:148
	s_waitcnt lgkmcnt(0)
	v_mfma_f32_16x16x4_f32 a[0:3], v46, v48, a[0:3]
	v_mfma_f32_16x16x4_f32 a[4:7], v54, v49, a[4:7]
	v_mfma_f32_16x16x4_f32 a[0:3], v51, v42, a[0:3]
	v_mfma_f32_16x16x4_f32 a[4:7], v53, v43, a[4:7]
	ds_read2_b32 v[42:43], v67 offset0:24 offset1:28
	v_mfma_f32_16x16x4_f32 a[0:3], v47, v44, a[0:3]
	ds_read2_b32 v[46:47], v67 offset0:216 offset1:220
	v_mfma_f32_16x16x4_f32 a[4:7], v55, v45, a[4:7]
	ds_read2_b32 v[44:45], v67 offset0:88 offset1:92
	s_waitcnt lgkmcnt(2)
	v_mfma_f32_16x16x4_f32 a[0:3], v42, v38, a[0:3]
	s_waitcnt lgkmcnt(0)
	v_mfma_f32_16x16x4_f32 a[4:7], v44, v39, a[4:7]
	ds_read2_b32 v[38:39], v67 offset0:152 offset1:156
	s_waitcnt lgkmcnt(0)
	v_mfma_f32_16x16x4_f32 a[0:3], v38, v40, a[0:3]
	v_mfma_f32_16x16x4_f32 a[4:7], v46, v41, a[4:7]
	v_mfma_f32_16x16x4_f32 a[0:3], v43, v34, a[0:3]
	v_mfma_f32_16x16x4_f32 a[4:7], v45, v35, a[4:7]
	ds_read2_b32 v[34:35], v67 offset0:32 offset1:36
	v_mfma_f32_16x16x4_f32 a[0:3], v39, v36, a[0:3]
	ds_read2_b32 v[38:39], v67 offset0:224 offset1:228
	v_mfma_f32_16x16x4_f32 a[4:7], v47, v37, a[4:7]
	ds_read2_b32 v[36:37], v67 offset0:96 offset1:100
	s_waitcnt lgkmcnt(2)
	v_mfma_f32_16x16x4_f32 a[0:3], v34, v30, a[0:3]
	s_waitcnt lgkmcnt(0)
	v_mfma_f32_16x16x4_f32 a[4:7], v36, v31, a[4:7]
	ds_read2_b32 v[30:31], v67 offset0:160 offset1:164
	s_waitcnt lgkmcnt(0)
	v_mfma_f32_16x16x4_f32 a[0:3], v30, v32, a[0:3]
	v_mfma_f32_16x16x4_f32 a[4:7], v38, v33, a[4:7]
	v_mfma_f32_16x16x4_f32 a[0:3], v35, v26, a[0:3]
	v_mfma_f32_16x16x4_f32 a[4:7], v37, v27, a[4:7]
	ds_read2_b32 v[26:27], v67 offset0:40 offset1:44
	v_mfma_f32_16x16x4_f32 a[0:3], v31, v28, a[0:3]
	ds_read2_b32 v[30:31], v67 offset0:232 offset1:236
	v_mfma_f32_16x16x4_f32 a[4:7], v39, v29, a[4:7]
	ds_read2_b32 v[28:29], v67 offset0:104 offset1:108
	s_waitcnt lgkmcnt(2)
	v_mfma_f32_16x16x4_f32 a[0:3], v26, v22, a[0:3]
	s_waitcnt lgkmcnt(0)
	v_mfma_f32_16x16x4_f32 a[4:7], v28, v23, a[4:7]
	ds_read2_b32 v[22:23], v67 offset0:168 offset1:172
	s_waitcnt lgkmcnt(0)
	v_mfma_f32_16x16x4_f32 a[0:3], v22, v24, a[0:3]
	v_mfma_f32_16x16x4_f32 a[4:7], v30, v25, a[4:7]
	v_mfma_f32_16x16x4_f32 a[0:3], v27, v18, a[0:3]
	v_mfma_f32_16x16x4_f32 a[4:7], v29, v19, a[4:7]
	ds_read2_b32 v[18:19], v67 offset0:48 offset1:52
	v_mfma_f32_16x16x4_f32 a[0:3], v23, v20, a[0:3]
	ds_read2_b32 v[22:23], v67 offset0:240 offset1:244
	v_mfma_f32_16x16x4_f32 a[4:7], v31, v21, a[4:7]
	ds_read2_b32 v[20:21], v67 offset0:112 offset1:116
	s_waitcnt lgkmcnt(2)
	v_mfma_f32_16x16x4_f32 a[0:3], v18, v14, a[0:3]
	s_waitcnt lgkmcnt(0)
	v_mfma_f32_16x16x4_f32 a[4:7], v20, v15, a[4:7]
	ds_read2_b32 v[14:15], v67 offset0:176 offset1:180
	s_waitcnt lgkmcnt(0)
	v_mfma_f32_16x16x4_f32 a[0:3], v14, v16, a[0:3]
	v_mfma_f32_16x16x4_f32 a[4:7], v22, v17, a[4:7]
	v_mfma_f32_16x16x4_f32 a[0:3], v19, v10, a[0:3]
	v_mfma_f32_16x16x4_f32 a[4:7], v21, v11, a[4:7]
	ds_read2_b32 v[10:11], v67 offset0:56 offset1:60
	v_mfma_f32_16x16x4_f32 a[0:3], v15, v12, a[0:3]
	ds_read2_b32 v[14:15], v67 offset0:248 offset1:252
	v_mfma_f32_16x16x4_f32 a[4:7], v23, v13, a[4:7]
	ds_read2_b32 v[12:13], v67 offset0:120 offset1:124
	s_waitcnt lgkmcnt(2)
	v_mfma_f32_16x16x4_f32 a[0:3], v10, v6, a[0:3]
	s_waitcnt lgkmcnt(0)
	v_mfma_f32_16x16x4_f32 a[4:7], v12, v7, a[4:7]
	ds_read2_b32 v[6:7], v67 offset0:184 offset1:188
	s_waitcnt lgkmcnt(0)
	v_mfma_f32_16x16x4_f32 a[0:3], v6, v8, a[0:3]
	v_mfma_f32_16x16x4_f32 a[4:7], v14, v9, a[4:7]
	v_mfma_f32_16x16x4_f32 a[0:3], v11, v2, a[0:3]
	v_mov_b32_e32 v2, 0x11300
	v_lshl_add_u32 v2, v134, 2, v2
	ds_read_b32 v2, v2
	v_mfma_f32_16x16x4_f32 a[4:7], v13, v3, a[4:7]
	v_lshlrev_b32_e32 v3, 10, v140
	v_add3_u32 v3, s0, v66, v3
	v_mfma_f32_16x16x4_f32 a[0:3], v7, v4, a[0:3]
	v_or_b32_e32 v7, s29, v140
	v_lshl_or_b32 v4, v7, 8, v66
	v_add_u32_e32 v4, 0x10100, v4
	v_mfma_f32_16x16x4_f32 a[4:7], v15, v5, a[4:7]
	s_nop 9
	v_accvgpr_read_b32 v5, a0
	v_accvgpr_read_b32 v6, a1
	v_accvgpr_read_b32 v8, a2
	v_accvgpr_read_b32 v9, a3
	v_accvgpr_read_b32 v70, a4
	v_accvgpr_read_b32 v71, a5
	v_accvgpr_read_b32 v72, a6
	v_accvgpr_read_b32 v73, a7
	v_add_f32_e32 v5, v5, v70
	v_add_f32_e32 v6, v6, v71
	v_add_f32_e32 v8, v8, v72
	v_add_f32_e32 v9, v9, v73
	s_waitcnt lgkmcnt(0)
	v_fma_f32 v5, -2.0, v5, v2
	v_fma_f32 v6, -2.0, v6, v2
	v_fma_f32 v8, -2.0, v8, v2
	v_fmac_f32_e32 v2, -2.0, v9
	ds_write2st64_b32 v3, v5, v6 offset1:1
	ds_write2st64_b32 v3, v8, v2 offset0:2 offset1:3
	s_waitcnt lgkmcnt(0)
	s_barrier
	ds_read2_b32 v[2:3], v4 offset1:16
	ds_read2_b32 v[4:5], v4 offset0:32 offset1:48
	v_or_b32_e32 v6, 16, v138
	v_or_b32_e32 v8, 32, v138
	v_or_b32_e32 v9, 48, v138
	s_waitcnt lgkmcnt(1)
	v_cmp_lt_f32_e32 vcc, v3, v2
	s_nop 1
	v_cndmask_b32_e32 v10, v2, v3, vcc
	v_cndmask_b32_e32 v6, v138, v6, vcc
	s_waitcnt lgkmcnt(0)
	v_cmp_lt_f32_e32 vcc, v4, v10
	s_nop 1
	v_cndmask_b32_e32 v10, v10, v4, vcc
	v_cndmask_b32_e32 v8, v6, v8, vcc
	v_cmp_lt_f32_e32 vcc, v5, v10
	s_nop 1
	v_cndmask_b32_e32 v6, v10, v5, vcc
	v_cndmask_b32_e32 v14, v8, v9, vcc
	s_nop 0
	v_mov_b32_dpp v9, v6 quad_perm:[1,0,3,2] row_mask:0xf bank_mask:0xf bound_ctrl:1
	v_mov_b32_dpp v8, v14 quad_perm:[1,0,3,2] row_mask:0xf bank_mask:0xf bound_ctrl:1
	v_cmp_gt_f32_e64 s[4:5], v6, v9
	v_cmp_ngt_f32_e32 vcc, v6, v9
	s_and_saveexec_b64 s[6:7], vcc
	v_cmp_eq_f32_e32 vcc, v6, v9
	v_cmp_lt_i32_e64 s[0:1], v8, v14
	s_and_b64 s[0:1], vcc, s[0:1]
	s_andn2_b64 s[4:5], s[4:5], exec
	s_and_b64 s[0:1], s[0:1], exec
	s_or_b64 s[4:5], s[4:5], s[0:1]
	s_or_b64 exec, exec, s[6:7]
	s_and_saveexec_b64 s[0:1], s[4:5]
	v_mov_b32_e32 v6, v9
	v_mov_b32_e32 v14, v8
	s_or_b64 exec, exec, s[0:1]
	v_mov_b32_dpp v9, v6 quad_perm:[2,3,0,1] row_mask:0xf bank_mask:0xf bound_ctrl:1
	v_mov_b32_dpp v8, v14 quad_perm:[2,3,0,1] row_mask:0xf bank_mask:0xf bound_ctrl:1
	v_cmp_gt_f32_e64 s[4:5], v6, v9
	v_cmp_ngt_f32_e32 vcc, v6, v9
	s_and_saveexec_b64 s[6:7], vcc
	v_cmp_eq_f32_e32 vcc, v6, v9
	v_cmp_lt_i32_e64 s[0:1], v8, v14
	s_and_b64 s[0:1], vcc, s[0:1]
	s_andn2_b64 s[4:5], s[4:5], exec
	s_and_b64 s[0:1], s[0:1], exec
	s_or_b64 s[4:5], s[4:5], s[0:1]
	s_or_b64 exec, exec, s[6:7]
	s_and_saveexec_b64 s[0:1], s[4:5]
	v_mov_b32_e32 v6, v9
	v_mov_b32_e32 v14, v8
	s_or_b64 exec, exec, s[0:1]
	v_mov_b32_dpp v9, v6 row_half_mirror row_mask:0xf bank_mask:0xf bound_ctrl:1
	v_mov_b32_dpp v8, v14 row_half_mirror row_mask:0xf bank_mask:0xf bound_ctrl:1
	v_cmp_gt_f32_e64 s[4:5], v6, v9
	v_cmp_ngt_f32_e32 vcc, v6, v9
	s_and_saveexec_b64 s[6:7], vcc
	v_cmp_eq_f32_e32 vcc, v6, v9
	v_cmp_lt_i32_e64 s[0:1], v8, v14
	s_and_b64 s[0:1], vcc, s[0:1]
	s_andn2_b64 s[4:5], s[4:5], exec
	s_and_b64 s[0:1], s[0:1], exec
	s_or_b64 s[4:5], s[4:5], s[0:1]
	s_or_b64 exec, exec, s[6:7]
	s_and_saveexec_b64 s[0:1], s[4:5]
	v_mov_b32_e32 v6, v9
	v_mov_b32_e32 v14, v8
	s_or_b64 exec, exec, s[0:1]
	v_mov_b32_dpp v8, v6 row_mirror row_mask:0xf bank_mask:0xf bound_ctrl:1
	v_mov_b32_dpp v9, v14 row_mirror row_mask:0xf bank_mask:0xf bound_ctrl:1
	v_cmp_gt_f32_e64 s[4:5], v6, v8
	v_cmp_ngt_f32_e32 vcc, v6, v8
	s_and_saveexec_b64 s[6:7], vcc
	v_cmp_eq_f32_e32 vcc, v6, v8
	v_cmp_lt_i32_e64 s[0:1], v9, v14
	s_and_b64 s[0:1], vcc, s[0:1]
	s_andn2_b64 s[4:5], s[4:5], exec
	s_and_b64 s[0:1], s[0:1], exec
	s_or_b64 s[4:5], s[4:5], s[0:1]
	s_or_b64 exec, exec, s[6:7]
	s_and_saveexec_b64 s[0:1], s[4:5]
	v_mov_b32_e32 v6, v8
	v_mov_b32_e32 v14, v9
	s_or_b64 exec, exec, s[0:1]
	v_mov_b32_e32 v8, 0x11300
	v_lshl_or_b32 v8, v1, 2, v8
	ds_read_b32 v8, v8
	v_mov_b32_e32 v9, 0x11200
	v_lshl_add_u32 v7, v7, 2, v9
	ds_read_b32 v9, v7
	v_mov_b32_e32 v13, 0x260
	s_waitcnt lgkmcnt(1)
	v_mov_b32_dpp v7, v8 quad_perm:[1,0,3,2] row_mask:0xf bank_mask:0xf bound_ctrl:1
	v_max_f32_e32 v8, v8, v8
	v_max_f32_e32 v7, v7, v7
	v_max_f32_e32 v7, v8, v7
	v_lshlrev_b32_e32 v18, 2, v139
	v_mov_b32_e32 v19, 0
	v_mov_b32_dpp v8, v7 quad_perm:[2,3,0,1] row_mask:0xf bank_mask:0xf bound_ctrl:1
	v_max_f32_e32 v8, v8, v8
	v_max_f32_e32 v7, v7, v8
	s_mov_b32 s25, 0
	s_mov_b32 s26, s25
	v_mov_b32_dpp v8, v7 row_half_mirror row_mask:0xf bank_mask:0xf bound_ctrl:1
	v_max_f32_e32 v8, v8, v8
	v_max_f32_e32 v7, v7, v8
	s_nop 1
	v_mov_b32_dpp v8, v7 row_mirror row_mask:0xf bank_mask:0xf bound_ctrl:1
	v_max_f32_e32 v8, v8, v8
	v_max_f32_e32 v7, v7, v8
	s_nop 0
	v_readlane_b32 s4, v7, 32
	v_readlane_b32 s5, v7, 48
	v_readlane_b32 s0, v7, 0
	v_readlane_b32 s1, v7, 16
	v_max_f32_e64 v7, s5, s5
	v_max_f32_e64 v8, s4, s4
	v_max_f32_e32 v7, v8, v7
	v_mov_b32_e32 v8, s1
	v_max3_f32 v8, s0, v8, v7
	s_mov_b32 s0, 0x3f800347
	s_mov_b32 s1, 0x3f8020c5
	s_waitcnt lgkmcnt(0)
	v_pk_mul_f32 v[8:9], v[8:9], s[0:1]
	s_mov_b32 s4, 0xf800000
	v_mul_f32_e32 v7, 0x4f800000, v9
	v_cmp_gt_f32_e32 vcc, s4, v9
	s_nop 1
	v_cndmask_b32_e32 v7, v9, v7, vcc
	v_sqrt_f32_e32 v10, v7
	s_nop 0
	v_add_u32_e32 v11, -1, v10
	v_fma_f32 v12, -v11, v10, v7
	v_cmp_ge_f32_e64 s[0:1], 0, v12
	v_add_u32_e32 v12, 1, v10
	s_nop 0
	v_cndmask_b32_e64 v11, v10, v11, s[0:1]
	v_fma_f32 v10, -v12, v10, v7
	v_cmp_lt_f32_e64 s[0:1], 0, v10
	s_nop 1
	v_cndmask_b32_e64 v10, v11, v12, s[0:1]
	v_mul_f32_e32 v11, 0x37800000, v10
	v_cndmask_b32_e32 v10, v10, v11, vcc
	v_mul_f32_e32 v11, 0x4f800000, v8
	v_cmp_gt_f32_e32 vcc, s4, v8
	v_cmp_class_f32_e64 s[0:1], v7, v13
	s_nop 0
	v_cndmask_b32_e32 v11, v8, v11, vcc
	v_sqrt_f32_e32 v12, v11
	v_cndmask_b32_e64 v7, v10, v7, s[0:1]
	v_add_u32_e32 v10, -1, v12
	v_fma_f32 v15, -v10, v12, v11
	v_cmp_ge_f32_e64 s[0:1], 0, v15
	v_add_u32_e32 v15, 1, v12
	s_nop 0
	v_cndmask_b32_e64 v10, v12, v10, s[0:1]
	v_fma_f32 v12, -v15, v12, v11
	v_cmp_lt_f32_e64 s[0:1], 0, v12
	s_nop 1
	v_cndmask_b32_e64 v10, v10, v15, s[0:1]
	v_mul_f32_e32 v12, 0x37800000, v10
	v_cndmask_b32_e32 v10, v10, v12, vcc
	v_cmp_class_f32_e32 vcc, v11, v13
	s_mov_b32 s0, 0x380637bd
	s_mov_b32 s1, 0x350637bd
	v_cndmask_b32_e32 v10, v10, v11, vcc
	v_mul_f32_e32 v7, v7, v10
	v_mul_f32_e32 v7, 0x3f800347, v7
	v_pk_mul_f32 v[8:9], v[8:9], s[0:1]
	s_nop 0
	v_fmamk_f32 v7, v7, 0x3888509c, v9
	v_add_f32_e32 v7, v8, v7
	v_add_f32_e32 v7, 0xda24260, v7
	v_add_f32_e32 v6, v6, v7
	v_cmp_le_f32_e64 s[8:9], v2, v6
	v_cmp_le_f32_e64 s[6:7], v3, v6
	v_cmp_le_f32_e64 s[4:5], v4, v6
	v_lshl_add_u64 v[2:3], s[22:23], 0, v[18:19]
	s_and_b32 s19, s8, 0xffff
	s_lshl_b32 s22, s6, 16
	v_cmp_le_f32_e64 s[0:1], v5, v6
	s_or_b32 s24, s19, s22
	s_and_b32 s23, s4, 0xffff
	s_mov_b32 s22, s25
	s_or_b64 s[22:23], s[24:25], s[22:23]
	s_lshl_b32 s27, s0, 16
	s_or_b64 s[26:27], s[22:23], s[26:27]
	s_add_u32 s22, s26, -1
	s_addc_u32 s23, s27, -1
	s_and_b64 s[22:23], s[26:27], s[22:23]
	s_cmp_eq_u64 s[22:23], 0
	v_readlane_b32 s22, v14, 0
	s_cbranch_scc1 .LBB0_139
	s_mov_b64 s[92:93], s[26:27]
